# LN1: the xor-1/2/4/8 steps of the two per-row wave reductions (both row paths) also use DPP moves instead of ds_bpermute
# speedup vs baseline: 1.0034x; 1.0034x over previous
.LBB0_1573:
	v_cvt_pk_f32_fp8_e32 v[96:97], v76
	v_cvt_pk_f32_fp8_sdwa v[98:99], v76 src0_sel:WORD_1
	v_cvt_pk_f32_fp8_e32 v[100:101], v92
	v_cvt_pk_f32_fp8_sdwa v[102:103], v92 src0_sel:WORD_1
	v_lshlrev_b32_e32 v104, 16, v60
	v_and_b32_e32 v105, 0xffff0000, v60
	v_pk_add_f32 v[96:97], v[96:97], v[100:101]
	v_pk_add_f32 v[98:99], v[98:99], v[102:103]
	v_pk_mul_f32 v[96:97], v[96:97], s[22:23] op_sel_hi:[1,0]
	v_lshlrev_b32_e32 v100, 16, v61
	v_and_b32_e32 v101, 0xffff0000, v61
	v_pk_mul_f32 v[98:99], v[98:99], s[22:23] op_sel_hi:[1,0]
	v_pk_fma_f32 v[96:97], v[104:105], s[20:21], v[96:97] op_sel_hi:[1,0,1]
	v_pk_fma_f32 v[98:99], v[100:101], s[20:21], v[98:99] op_sel_hi:[1,0,1]
	v_cvt_pk_f32_fp8_e32 v[100:101], v77
	v_cvt_pk_f32_fp8_sdwa v[102:103], v77 src0_sel:WORD_1
	v_cvt_pk_f32_fp8_e32 v[104:105], v93
	v_cvt_pk_f32_fp8_sdwa v[106:107], v93 src0_sel:WORD_1
	v_lshlrev_b32_e32 v108, 16, v62
	v_and_b32_e32 v109, 0xffff0000, v62
	v_pk_add_f32 v[100:101], v[100:101], v[104:105]
	v_pk_add_f32 v[102:103], v[102:103], v[106:107]
	v_pk_mul_f32 v[100:101], v[100:101], s[22:23] op_sel_hi:[1,0]
	v_lshlrev_b32_e32 v104, 16, v63
	v_and_b32_e32 v105, 0xffff0000, v63
	v_pk_mul_f32 v[102:103], v[102:103], s[22:23] op_sel_hi:[1,0]
	v_pk_fma_f32 v[100:101], v[108:109], s[20:21], v[100:101] op_sel_hi:[1,0,1]
	v_pk_fma_f32 v[102:103], v[104:105], s[20:21], v[102:103] op_sel_hi:[1,0,1]
	v_cvt_pk_f32_fp8_e32 v[104:105], v72
	v_cvt_pk_f32_fp8_sdwa v[106:107], v72 src0_sel:WORD_1
	v_cvt_pk_f32_fp8_e32 v[108:109], v88
	v_cvt_pk_f32_fp8_sdwa v[110:111], v88 src0_sel:WORD_1
	v_lshlrev_b32_e32 v112, 16, v56
	v_and_b32_e32 v113, 0xffff0000, v56
	v_pk_add_f32 v[104:105], v[104:105], v[108:109]
	v_pk_add_f32 v[106:107], v[106:107], v[110:111]
	v_pk_mul_f32 v[104:105], v[104:105], s[22:23] op_sel_hi:[1,0]
	v_lshlrev_b32_e32 v108, 16, v57
	v_and_b32_e32 v109, 0xffff0000, v57
	v_pk_mul_f32 v[106:107], v[106:107], s[22:23] op_sel_hi:[1,0]
	v_pk_fma_f32 v[104:105], v[112:113], s[20:21], v[104:105] op_sel_hi:[1,0,1]
	v_pk_fma_f32 v[106:107], v[108:109], s[20:21], v[106:107] op_sel_hi:[1,0,1]
	v_cvt_pk_f32_fp8_e32 v[108:109], v73
	v_cvt_pk_f32_fp8_sdwa v[110:111], v73 src0_sel:WORD_1
	v_cvt_pk_f32_fp8_e32 v[112:113], v89
	v_cvt_pk_f32_fp8_sdwa v[114:115], v89 src0_sel:WORD_1
	v_lshlrev_b32_e32 v116, 16, v58
	v_and_b32_e32 v117, 0xffff0000, v58
	v_pk_add_f32 v[108:109], v[108:109], v[112:113]
	v_pk_add_f32 v[110:111], v[110:111], v[114:115]
	v_pk_mul_f32 v[108:109], v[108:109], s[22:23] op_sel_hi:[1,0]
	v_lshlrev_b32_e32 v112, 16, v59
	v_and_b32_e32 v113, 0xffff0000, v59
	v_pk_mul_f32 v[110:111], v[110:111], s[22:23] op_sel_hi:[1,0]
	v_pk_fma_f32 v[108:109], v[116:117], s[20:21], v[108:109] op_sel_hi:[1,0,1]
	v_pk_fma_f32 v[110:111], v[112:113], s[20:21], v[110:111] op_sel_hi:[1,0,1]
	v_cvt_pk_f32_fp8_e32 v[112:113], v68
	v_cvt_pk_f32_fp8_sdwa v[114:115], v68 src0_sel:WORD_1
	v_cvt_pk_f32_fp8_e32 v[116:117], v84
	v_cvt_pk_f32_fp8_sdwa v[118:119], v84 src0_sel:WORD_1
	v_lshlrev_b32_e32 v120, 16, v52
	v_and_b32_e32 v121, 0xffff0000, v52
	v_pk_add_f32 v[112:113], v[112:113], v[116:117]
	v_pk_add_f32 v[114:115], v[114:115], v[118:119]
	v_pk_mul_f32 v[112:113], v[112:113], s[22:23] op_sel_hi:[1,0]
	v_lshlrev_b32_e32 v116, 16, v53
	v_and_b32_e32 v117, 0xffff0000, v53
	v_pk_mul_f32 v[114:115], v[114:115], s[22:23] op_sel_hi:[1,0]
	v_pk_fma_f32 v[112:113], v[120:121], s[20:21], v[112:113] op_sel_hi:[1,0,1]
	v_pk_fma_f32 v[114:115], v[116:117], s[20:21], v[114:115] op_sel_hi:[1,0,1]
	v_cvt_pk_f32_fp8_e32 v[116:117], v69
	v_cvt_pk_f32_fp8_sdwa v[118:119], v69 src0_sel:WORD_1
	v_cvt_pk_f32_fp8_e32 v[120:121], v85
	v_cvt_pk_f32_fp8_sdwa v[122:123], v85 src0_sel:WORD_1
	v_lshlrev_b32_e32 v124, 16, v54
	v_and_b32_e32 v125, 0xffff0000, v54
	v_pk_add_f32 v[116:117], v[116:117], v[120:121]
	v_pk_add_f32 v[118:119], v[118:119], v[122:123]
	v_pk_mul_f32 v[116:117], v[116:117], s[22:23] op_sel_hi:[1,0]
	v_lshlrev_b32_e32 v120, 16, v55
	v_and_b32_e32 v121, 0xffff0000, v55
	v_pk_mul_f32 v[118:119], v[118:119], s[22:23] op_sel_hi:[1,0]
	v_pk_fma_f32 v[116:117], v[124:125], s[20:21], v[116:117] op_sel_hi:[1,0,1]
	v_pk_fma_f32 v[118:119], v[120:121], s[20:21], v[118:119] op_sel_hi:[1,0,1]
	v_cvt_pk_f32_fp8_e32 v[120:121], v64
	v_cvt_pk_f32_fp8_sdwa v[122:123], v64 src0_sel:WORD_1
	v_cvt_pk_f32_fp8_e32 v[124:125], v80
	v_cvt_pk_f32_fp8_sdwa v[126:127], v80 src0_sel:WORD_1
	v_lshlrev_b32_e32 v138, 16, v48
	v_and_b32_e32 v139, 0xffff0000, v48
	v_pk_add_f32 v[120:121], v[120:121], v[124:125]
	v_pk_add_f32 v[122:123], v[122:123], v[126:127]
	v_pk_mul_f32 v[120:121], v[120:121], s[22:23] op_sel_hi:[1,0]
	v_lshlrev_b32_e32 v124, 16, v49
	v_and_b32_e32 v125, 0xffff0000, v49
	v_pk_mul_f32 v[122:123], v[122:123], s[22:23] op_sel_hi:[1,0]
	v_cvt_pk_f32_fp8_sdwa v[126:127], v65 src0_sel:WORD_1
	v_cvt_pk_f32_fp8_sdwa v[156:157], v81 src0_sel:WORD_1
	v_pk_fma_f32 v[120:121], v[138:139], s[20:21], v[120:121] op_sel_hi:[1,0,1]
	v_pk_fma_f32 v[122:123], v[124:125], s[20:21], v[122:123] op_sel_hi:[1,0,1]
	v_cvt_pk_f32_fp8_e32 v[124:125], v65
	v_cvt_pk_f32_fp8_e32 v[138:139], v81
	v_pk_add_f32 v[126:127], v[126:127], v[156:157]
	v_lshlrev_b32_e32 v158, 16, v50
	v_pk_mul_f32 v[126:127], v[126:127], s[22:23] op_sel_hi:[1,0]
	v_pk_add_f32 v[124:125], v[124:125], v[138:139]
	v_lshlrev_b32_e32 v138, 16, v51
	v_and_b32_e32 v139, 0xffff0000, v51
	v_pk_fma_f32 v[126:127], v[138:139], s[20:21], v[126:127] op_sel_hi:[1,0,1]
	v_add_f32_e32 v138, 0, v96
	v_add_f32_e32 v138, v97, v138
	v_add_f32_e32 v138, v98, v138
	v_add_f32_e32 v138, v99, v138
	v_add_f32_e32 v138, v138, v100
	v_add_f32_e32 v138, v101, v138
	v_add_f32_e32 v138, v102, v138
	v_add_f32_e32 v138, v103, v138
	v_add_f32_e32 v138, v138, v104
	v_add_f32_e32 v138, v105, v138
	v_add_f32_e32 v138, v106, v138
	v_add_f32_e32 v138, v107, v138
	v_add_f32_e32 v138, v138, v108
	v_add_f32_e32 v138, v109, v138
	v_add_f32_e32 v138, v110, v138
	v_add_f32_e32 v138, v111, v138
	v_add_f32_e32 v138, v138, v112
	v_add_f32_e32 v138, v113, v138
	v_add_f32_e32 v138, v114, v138
	v_add_f32_e32 v138, v115, v138
	v_add_f32_e32 v138, v138, v116
	v_add_f32_e32 v138, v117, v138
	v_add_f32_e32 v138, v118, v138
	v_add_f32_e32 v138, v119, v138
	v_add_f32_e32 v138, v138, v120
	v_add_f32_e32 v138, v121, v138
	v_and_b32_e32 v159, 0xffff0000, v50
	v_pk_mul_f32 v[124:125], v[124:125], s[22:23] op_sel_hi:[1,0]
	v_add_f32_e32 v138, v122, v138
	v_pk_fma_f32 v[124:125], v[158:159], s[20:21], v[124:125] op_sel_hi:[1,0,1]
	v_add_f32_e32 v138, v123, v138
	v_and_b32_e32 v139, 64, v195
	v_add_f32_e32 v138, v138, v124
	v_add_u32_e32 v139, 64, v139
	v_xor_b32_e32 v155, 1, v195
	v_add_f32_e32 v138, v125, v138
	v_cmp_lt_i32_e32 vcc, v155, v139
	v_add_f32_e32 v138, v126, v138
	v_add_f32_e32 v138, v127, v138
	v_cndmask_b32_e32 v155, v195, v155, vcc
	v_lshlrev_b32_e32 v155, 2, v155
	s_nop 1
	v_mov_b32_dpp v156, v138 quad_perm:[1,0,3,2] row_mask:0xf bank_mask:0xf
	s_waitcnt lgkmcnt(0)
	v_add_f32_e32 v138, v138, v156
	v_xor_b32_e32 v156, 2, v195
	v_cmp_lt_i32_e32 vcc, v156, v139
	s_nop 1
	v_cndmask_b32_e32 v156, v195, v156, vcc
	v_lshlrev_b32_e32 v156, 2, v156
	s_nop 1
	v_mov_b32_dpp v157, v138 quad_perm:[2,3,0,1] row_mask:0xf bank_mask:0xf
	s_waitcnt lgkmcnt(0)
	v_add_f32_e32 v138, v138, v157
	v_xor_b32_e32 v157, 4, v195
	v_cmp_lt_i32_e32 vcc, v157, v139
	s_nop 1
	v_cndmask_b32_e32 v157, v195, v157, vcc
	v_lshlrev_b32_e32 v157, 2, v157
	s_nop 1
	v_mov_b32_dpp v158, v138 row_half_mirror row_mask:0xf bank_mask:0xf
	s_waitcnt lgkmcnt(0)
	v_add_f32_e32 v138, v138, v158
	v_xor_b32_e32 v158, 8, v195
	v_cmp_lt_i32_e32 vcc, v158, v139
	s_nop 1
	v_cndmask_b32_e32 v158, v195, v158, vcc
	v_lshlrev_b32_e32 v158, 2, v158
	s_nop 1
	v_mov_b32_dpp v159, v138 row_mirror row_mask:0xf bank_mask:0xf
	s_waitcnt lgkmcnt(0)
	v_add_f32_e32 v138, v138, v159
	v_xor_b32_e32 v159, 16, v195
	v_cmp_lt_i32_e32 vcc, v159, v139
	s_nop 1
	v_cndmask_b32_e32 v159, v195, v159, vcc
	v_lshlrev_b32_e32 v159, 2, v159
	ds_bpermute_b32 v160, v159, v138
	s_waitcnt lgkmcnt(0)
	v_add_f32_e32 v138, v138, v160
	v_xor_b32_e32 v160, 32, v195
	v_cmp_lt_i32_e32 vcc, v160, v139
	s_nop 1
	v_cndmask_b32_e32 v139, v195, v160, vcc
	v_lshlrev_b32_e32 v160, 2, v139
	ds_bpermute_b32 v139, v160, v138
	s_waitcnt lgkmcnt(0)
	v_add_f32_e32 v138, v138, v139
	v_mul_f32_e32 v138, 0x3a000000, v138
	v_pk_add_f32 v[184:185], v[96:97], v[138:139] op_sel_hi:[1,0] neg_lo:[0,1] neg_hi:[0,1]
	v_pk_add_f32 v[188:189], v[98:99], v[138:139] op_sel_hi:[1,0] neg_lo:[0,1] neg_hi:[0,1]
	v_pk_mul_f32 v[96:97], v[184:185], v[184:185]
	v_pk_mul_f32 v[98:99], v[188:189], v[188:189]
	v_add_f32_e32 v96, v96, v97
	v_pk_add_f32 v[214:215], v[100:101], v[138:139] op_sel_hi:[1,0] neg_lo:[0,1] neg_hi:[0,1]
	v_add_f32_e32 v96, v98, v96
	v_pk_mul_f32 v[100:101], v[214:215], v[214:215]
	v_add_f32_e32 v96, v99, v96
	v_pk_add_f32 v[216:217], v[102:103], v[138:139] op_sel_hi:[1,0] neg_lo:[0,1] neg_hi:[0,1]
	v_add_f32_e32 v96, v100, v96
	v_pk_mul_f32 v[102:103], v[216:217], v[216:217]
	v_add_f32_e32 v96, v101, v96
	v_pk_add_f32 v[218:219], v[104:105], v[138:139] op_sel_hi:[1,0] neg_lo:[0,1] neg_hi:[0,1]
	v_add_f32_e32 v96, v102, v96
	v_pk_mul_f32 v[104:105], v[218:219], v[218:219]
	v_add_f32_e32 v96, v103, v96
	v_pk_add_f32 v[220:221], v[106:107], v[138:139] op_sel_hi:[1,0] neg_lo:[0,1] neg_hi:[0,1]
	v_add_f32_e32 v96, v104, v96
	v_pk_mul_f32 v[106:107], v[220:221], v[220:221]
	v_add_f32_e32 v96, v105, v96
	v_pk_add_f32 v[222:223], v[108:109], v[138:139] op_sel_hi:[1,0] neg_lo:[0,1] neg_hi:[0,1]
	v_add_f32_e32 v96, v106, v96
	v_pk_mul_f32 v[108:109], v[222:223], v[222:223]
	v_add_f32_e32 v96, v107, v96
	v_pk_add_f32 v[224:225], v[110:111], v[138:139] op_sel_hi:[1,0] neg_lo:[0,1] neg_hi:[0,1]
	v_add_f32_e32 v96, v108, v96
	v_pk_mul_f32 v[110:111], v[224:225], v[224:225]
	v_add_f32_e32 v96, v109, v96
	v_pk_add_f32 v[226:227], v[112:113], v[138:139] op_sel_hi:[1,0] neg_lo:[0,1] neg_hi:[0,1]
	v_add_f32_e32 v96, v110, v96
	v_pk_mul_f32 v[112:113], v[226:227], v[226:227]
	v_add_f32_e32 v96, v111, v96
	v_pk_add_f32 v[228:229], v[114:115], v[138:139] op_sel_hi:[1,0] neg_lo:[0,1] neg_hi:[0,1]
	v_add_f32_e32 v96, v112, v96
	v_pk_mul_f32 v[114:115], v[228:229], v[228:229]
	v_add_f32_e32 v96, v113, v96
	v_pk_add_f32 v[230:231], v[116:117], v[138:139] op_sel_hi:[1,0] neg_lo:[0,1] neg_hi:[0,1]
	v_add_f32_e32 v96, v114, v96
	v_pk_mul_f32 v[116:117], v[230:231], v[230:231]
	v_add_f32_e32 v96, v115, v96
	v_pk_add_f32 v[232:233], v[118:119], v[138:139] op_sel_hi:[1,0] neg_lo:[0,1] neg_hi:[0,1]
	v_add_f32_e32 v96, v116, v96
	v_pk_mul_f32 v[118:119], v[232:233], v[232:233]
	v_add_f32_e32 v96, v117, v96
	v_pk_add_f32 v[234:235], v[120:121], v[138:139] op_sel_hi:[1,0] neg_lo:[0,1] neg_hi:[0,1]
	v_add_f32_e32 v96, v118, v96
	v_pk_mul_f32 v[120:121], v[234:235], v[234:235]
	v_add_f32_e32 v96, v119, v96
	v_pk_add_f32 v[236:237], v[122:123], v[138:139] op_sel_hi:[1,0] neg_lo:[0,1] neg_hi:[0,1]
	v_add_f32_e32 v96, v120, v96
	v_pk_mul_f32 v[122:123], v[236:237], v[236:237]
	v_add_f32_e32 v96, v121, v96
	v_pk_add_f32 v[238:239], v[124:125], v[138:139] op_sel_hi:[1,0] neg_lo:[0,1] neg_hi:[0,1]
	v_add_f32_e32 v96, v122, v96
	v_pk_mul_f32 v[124:125], v[238:239], v[238:239]
	v_add_f32_e32 v96, v123, v96
	v_pk_add_f32 v[138:139], v[126:127], v[138:139] op_sel_hi:[1,0] neg_lo:[0,1] neg_hi:[0,1]
	v_add_f32_e32 v96, v124, v96
	v_pk_mul_f32 v[126:127], v[138:139], v[138:139]
	v_add_f32_e32 v96, v125, v96
	v_add_f32_e32 v96, v126, v96
	v_add_f32_e32 v96, v127, v96
	s_nop 1
	v_mov_b32_dpp v97, v96 quad_perm:[1,0,3,2] row_mask:0xf bank_mask:0xf
	s_waitcnt lgkmcnt(0)
	v_add_f32_e32 v96, v96, v97
	s_nop 1
	v_mov_b32_dpp v97, v96 quad_perm:[2,3,0,1] row_mask:0xf bank_mask:0xf
	s_waitcnt lgkmcnt(0)
	v_add_f32_e32 v96, v96, v97
	s_nop 1
	v_mov_b32_dpp v97, v96 row_half_mirror row_mask:0xf bank_mask:0xf
	s_waitcnt lgkmcnt(0)
	v_add_f32_e32 v96, v96, v97
	s_nop 1
	v_mov_b32_dpp v97, v96 row_mirror row_mask:0xf bank_mask:0xf
	s_waitcnt lgkmcnt(0)
	v_add_f32_e32 v112, v96, v97
	ds_bpermute_b32 v113, v159, v112
	ds_read_b128 v[96:99], v134
	ds_read_b128 v[100:103], v135
	ds_read_b128 v[104:107], v136
	ds_read_b128 v[108:111], v142
	s_waitcnt lgkmcnt(4)
	v_add_f32_e32 v116, v112, v113
	ds_bpermute_b32 v117, v160, v116
	ds_read_b128 v[112:115], v143
	ds_read_b128 v[156:159], v144
	ds_read_b128 v[120:123], v145
	ds_read_b128 v[160:163], v146
	ds_read_b128 v[164:167], v147
	ds_read_b128 v[168:171], v148
	ds_read_b128 v[172:175], v149
	ds_read_b128 v[176:179], v150
	ds_read_b128 v[180:183], v151
	ds_read_b128 v[202:205], v152
	ds_read_b128 v[206:209], v153
	ds_read_b128 v[210:213], v154
	s_waitcnt lgkmcnt(12)
	v_add_f32_e32 v116, v116, v117
	v_fmamk_f32 v116, v116, 0x3a000000, v192
	v_mul_f32_e32 v117, 0x4f800000, v116
	v_cmp_gt_f32_e32 vcc, s88, v116
	s_nop 1
	v_cndmask_b32_e32 v116, v116, v117, vcc
	v_sqrt_f32_e32 v117, v116
	s_nop 0
	v_add_u32_e32 v118, -1, v117
	v_fma_f32 v119, -v118, v117, v116
	v_cmp_ge_f32_e64 s[36:37], 0, v119
	v_add_u32_e32 v119, 1, v117
	s_nop 0
	v_cndmask_b32_e64 v118, v117, v118, s[36:37]
	v_fma_f32 v117, -v119, v117, v116
	v_cmp_lt_f32_e64 s[36:37], 0, v117
	s_nop 1
	v_cndmask_b32_e64 v117, v118, v119, s[36:37]
	v_mul_f32_e32 v118, 0x37800000, v117
	v_cndmask_b32_e32 v117, v117, v118, vcc
	v_cmp_class_f32_e32 vcc, v116, v191
	s_nop 1
	v_cndmask_b32_e32 v116, v117, v116, vcc
	v_div_scale_f32 v117, s[12:13], v116, v116, 1.0
	v_rcp_f32_e32 v118, v117
	s_mov_b64 s[12:13], -1
	v_fma_f32 v119, -v117, v118, 1.0
	v_fmac_f32_e32 v118, v119, v118
	v_div_scale_f32 v119, vcc, 1.0, v116, 1.0
	v_mul_f32_e32 v124, v119, v118
	v_fma_f32 v125, -v117, v124, v119
	v_fmac_f32_e32 v124, v125, v118
	v_fma_f32 v117, -v117, v124, v119
	v_div_fmas_f32 v117, v117, v118, v124
	v_div_fixup_f32 v240, v117, v116, 1.0
	v_pk_mul_f32 v[116:117], v[184:185], v[240:241] op_sel_hi:[1,0]
	v_pk_mul_f32 v[118:119], v[214:215], v[240:241] op_sel_hi:[1,0]
	v_pk_fma_f32 v[124:125], v[96:97], v[116:117], v[104:105]
	v_pk_mul_f32 v[96:97], v[188:189], v[240:241] op_sel_hi:[1,0]
	v_pk_fma_f32 v[116:117], v[100:101], v[118:119], v[108:109]
	v_pk_fma_f32 v[126:127], v[98:99], v[96:97], v[106:107]
	v_pk_mul_f32 v[96:97], v[218:219], v[240:241] op_sel_hi:[1,0]
	v_pk_mul_f32 v[98:99], v[222:223], v[240:241] op_sel_hi:[1,0]
	s_waitcnt lgkmcnt(9)
	v_pk_fma_f32 v[120:121], v[112:113], v[96:97], v[120:121]
	s_waitcnt lgkmcnt(8)
	v_pk_fma_f32 v[112:113], v[156:157], v[98:99], v[160:161]
	v_pk_mul_f32 v[96:97], v[220:221], v[240:241] op_sel_hi:[1,0]
	v_pk_mul_f32 v[98:99], v[224:225], v[240:241] op_sel_hi:[1,0]
	v_pk_mul_f32 v[100:101], v[216:217], v[240:241] op_sel_hi:[1,0]
	v_pk_fma_f32 v[122:123], v[114:115], v[96:97], v[122:123]
	v_pk_fma_f32 v[114:115], v[158:159], v[98:99], v[162:163]
	v_pk_mul_f32 v[96:97], v[226:227], v[240:241] op_sel_hi:[1,0]
	v_pk_mul_f32 v[98:99], v[230:231], v[240:241] op_sel_hi:[1,0]
	v_pk_fma_f32 v[118:119], v[102:103], v[100:101], v[110:111]
	s_waitcnt lgkmcnt(5)
	v_pk_fma_f32 v[108:109], v[164:165], v[96:97], v[172:173]
	s_waitcnt lgkmcnt(4)
	v_pk_fma_f32 v[100:101], v[168:169], v[98:99], v[176:177]
	v_pk_mul_f32 v[96:97], v[228:229], v[240:241] op_sel_hi:[1,0]
	v_pk_mul_f32 v[98:99], v[232:233], v[240:241] op_sel_hi:[1,0]
	v_pk_fma_f32 v[110:111], v[166:167], v[96:97], v[174:175]
	v_pk_fma_f32 v[102:103], v[170:171], v[98:99], v[178:179]
	v_pk_mul_f32 v[96:97], v[234:235], v[240:241] op_sel_hi:[1,0]
	v_pk_mul_f32 v[98:99], v[238:239], v[240:241] op_sel_hi:[1,0]
	s_waitcnt lgkmcnt(1)
	v_pk_fma_f32 v[104:105], v[180:181], v[96:97], v[206:207]
	s_waitcnt lgkmcnt(0)
	v_pk_fma_f32 v[96:97], v[202:203], v[98:99], v[210:211]
	v_pk_mul_f32 v[98:99], v[236:237], v[240:241] op_sel_hi:[1,0]
	v_pk_mul_f32 v[138:139], v[138:139], v[240:241] op_sel_hi:[1,0]
	v_pk_fma_f32 v[106:107], v[182:183], v[98:99], v[208:209]
	v_pk_fma_f32 v[98:99], v[204:205], v[138:139], v[212:213]
	s_andn2_b64 vcc, exec, s[8:9]
	s_cbranch_vccnz .LBB0_1575
	s_ashr_i32 s7, s6, 31
	s_lshl_b64 s[12:13], s[6:7], 12
	v_lshl_add_u64 v[138:139], v[130:131], 0, s[12:13]
	v_cvt_pk_bf16_f32 v156, v124, v125
	v_cvt_pk_bf16_f32 v157, v126, v127
	v_cvt_pk_bf16_f32 v158, v116, v117
	v_cvt_pk_bf16_f32 v159, v118, v119
	global_store_dwordx4 v[138:139], v[156:159], off
	s_mov_b64 s[12:13], 0
	s_nop 0
	v_cvt_pk_bf16_f32 v156, v120, v121
	v_cvt_pk_bf16_f32 v157, v122, v123
	v_cvt_pk_bf16_f32 v158, v112, v113
	v_cvt_pk_bf16_f32 v159, v114, v115
	global_store_dwordx4 v[138:139], v[156:159], off offset:1024
	s_nop 1
	v_cvt_pk_bf16_f32 v156, v108, v109
	v_cvt_pk_bf16_f32 v157, v110, v111
	v_cvt_pk_bf16_f32 v158, v100, v101
	v_cvt_pk_bf16_f32 v159, v102, v103
	global_store_dwordx4 v[138:139], v[156:159], off offset:2048
	s_nop 1
	v_cvt_pk_bf16_f32 v156, v104, v105
	v_cvt_pk_bf16_f32 v157, v106, v107
	v_cvt_pk_bf16_f32 v158, v96, v97
	v_cvt_pk_bf16_f32 v159, v98, v99
	global_store_dwordx4 v[138:139], v[156:159], off offset:3072

.LBB0_1580:
	s_or_b32 s4, s62, 7
	s_mul_i32 s4, s4, s14
	s_add_i32 s6, s4, s59
	s_cmpk_gt_i32 s6, 0x3fff
	s_cbranch_scc1 .LBB0_1558
	s_waitcnt vmcnt(7)
	v_cvt_pk_f32_fp8_e32 v[108:109], v16
	s_waitcnt vmcnt(3)
	v_cvt_pk_f32_fp8_e32 v[110:111], v32
	v_cvt_pk_f32_fp8_sdwa v[104:105], v16 src0_sel:WORD_1
	v_cvt_pk_f32_fp8_sdwa v[106:107], v32 src0_sel:WORD_1
	v_cvt_pk_f32_fp8_e32 v[100:101], v17
	v_cvt_pk_f32_fp8_e32 v[102:103], v33
	v_pk_add_f32 v[108:109], v[108:109], v[110:111]
	v_lshlrev_b32_e32 v110, 16, v0
	v_pk_mul_f32 v[108:109], v[108:109], s[22:23] op_sel_hi:[1,0]
	v_and_b32_e32 v111, 0xffff0000, v0
	v_cvt_pk_f32_fp8_sdwa v[96:97], v17 src0_sel:WORD_1
	v_cvt_pk_f32_fp8_sdwa v[98:99], v33 src0_sel:WORD_1
	v_pk_fma_f32 v[108:109], v[110:111], s[20:21], v[108:109] op_sel_hi:[1,0,1]
	v_pk_add_f32 v[104:105], v[104:105], v[106:107]
	v_add_f32_e32 v110, 0, v108
	v_pk_mul_f32 v[104:105], v[104:105], s[22:23] op_sel_hi:[1,0]
	v_lshlrev_b32_e32 v106, 16, v1
	v_and_b32_e32 v107, 0xffff0000, v1
	v_cvt_pk_f32_fp8_e32 v[92:93], v20
	s_waitcnt vmcnt(2)
	v_cvt_pk_f32_fp8_e32 v[94:95], v36
	v_add_f32_e32 v110, v109, v110
	v_pk_fma_f32 v[104:105], v[106:107], s[20:21], v[104:105] op_sel_hi:[1,0,1]
	v_pk_add_f32 v[100:101], v[100:101], v[102:103]
	v_add_f32_e32 v106, v104, v110
	v_pk_mul_f32 v[100:101], v[100:101], s[22:23] op_sel_hi:[1,0]
	v_lshlrev_b32_e32 v102, 16, v2
	v_and_b32_e32 v103, 0xffff0000, v2
	v_cvt_pk_f32_fp8_sdwa v[88:89], v20 src0_sel:WORD_1
	v_cvt_pk_f32_fp8_sdwa v[90:91], v36 src0_sel:WORD_1
	v_add_f32_e32 v106, v105, v106
	v_pk_fma_f32 v[100:101], v[102:103], s[20:21], v[100:101] op_sel_hi:[1,0,1]
	v_pk_add_f32 v[96:97], v[96:97], v[98:99]
	v_add_f32_e32 v102, v100, v106
	v_pk_mul_f32 v[96:97], v[96:97], s[22:23] op_sel_hi:[1,0]
	v_lshlrev_b32_e32 v98, 16, v3
	v_and_b32_e32 v99, 0xffff0000, v3
	v_cvt_pk_f32_fp8_e32 v[84:85], v21
	v_cvt_pk_f32_fp8_e32 v[86:87], v37
	v_add_f32_e32 v102, v101, v102
	v_pk_fma_f32 v[96:97], v[98:99], s[20:21], v[96:97] op_sel_hi:[1,0,1]
	v_pk_add_f32 v[92:93], v[92:93], v[94:95]
	v_add_f32_e32 v98, v96, v102
	v_pk_mul_f32 v[92:93], v[92:93], s[22:23] op_sel_hi:[1,0]
	v_lshlrev_b32_e32 v94, 16, v4
	v_and_b32_e32 v95, 0xffff0000, v4
	v_cvt_pk_f32_fp8_sdwa v[80:81], v21 src0_sel:WORD_1
	v_cvt_pk_f32_fp8_sdwa v[82:83], v37 src0_sel:WORD_1
	v_add_f32_e32 v98, v97, v98
	v_pk_fma_f32 v[92:93], v[94:95], s[20:21], v[92:93] op_sel_hi:[1,0,1]
	v_pk_add_f32 v[88:89], v[88:89], v[90:91]
	v_add_f32_e32 v94, v92, v98
	v_pk_mul_f32 v[88:89], v[88:89], s[22:23] op_sel_hi:[1,0]
	v_lshlrev_b32_e32 v90, 16, v5
	v_and_b32_e32 v91, 0xffff0000, v5
	v_cvt_pk_f32_fp8_e32 v[76:77], v24
	s_waitcnt vmcnt(1)
	v_cvt_pk_f32_fp8_e32 v[78:79], v40
	v_add_f32_e32 v94, v93, v94
	v_pk_fma_f32 v[88:89], v[90:91], s[20:21], v[88:89] op_sel_hi:[1,0,1]
	v_pk_add_f32 v[84:85], v[84:85], v[86:87]
	v_add_f32_e32 v90, v88, v94
	v_pk_mul_f32 v[84:85], v[84:85], s[22:23] op_sel_hi:[1,0]
	v_lshlrev_b32_e32 v86, 16, v6
	v_and_b32_e32 v87, 0xffff0000, v6
	v_cvt_pk_f32_fp8_sdwa v[72:73], v24 src0_sel:WORD_1
	v_cvt_pk_f32_fp8_sdwa v[74:75], v40 src0_sel:WORD_1
	v_add_f32_e32 v90, v89, v90
	v_pk_fma_f32 v[84:85], v[86:87], s[20:21], v[84:85] op_sel_hi:[1,0,1]
	v_pk_add_f32 v[80:81], v[80:81], v[82:83]
	v_add_f32_e32 v86, v84, v90
	v_pk_mul_f32 v[80:81], v[80:81], s[22:23] op_sel_hi:[1,0]
	v_lshlrev_b32_e32 v82, 16, v7
	v_and_b32_e32 v83, 0xffff0000, v7
	v_cvt_pk_f32_fp8_e32 v[68:69], v25
	v_cvt_pk_f32_fp8_e32 v[70:71], v41
	v_add_f32_e32 v86, v85, v86
	v_pk_fma_f32 v[80:81], v[82:83], s[20:21], v[80:81] op_sel_hi:[1,0,1]
	v_pk_add_f32 v[76:77], v[76:77], v[78:79]
	v_add_f32_e32 v82, v80, v86
	v_pk_mul_f32 v[76:77], v[76:77], s[22:23] op_sel_hi:[1,0]
	v_lshlrev_b32_e32 v78, 16, v8
	v_and_b32_e32 v79, 0xffff0000, v8
	v_cvt_pk_f32_fp8_sdwa v[64:65], v25 src0_sel:WORD_1
	v_cvt_pk_f32_fp8_sdwa v[66:67], v41 src0_sel:WORD_1
	v_add_f32_e32 v82, v81, v82
	v_pk_fma_f32 v[76:77], v[78:79], s[20:21], v[76:77] op_sel_hi:[1,0,1]
	v_pk_add_f32 v[72:73], v[72:73], v[74:75]
	v_add_f32_e32 v78, v76, v82
	v_pk_mul_f32 v[72:73], v[72:73], s[22:23] op_sel_hi:[1,0]
	v_lshlrev_b32_e32 v74, 16, v9
	v_and_b32_e32 v75, 0xffff0000, v9
	v_cvt_pk_f32_fp8_e32 v[60:61], v28
	s_waitcnt vmcnt(0)
	v_cvt_pk_f32_fp8_e32 v[62:63], v44
	v_add_f32_e32 v78, v77, v78
	v_pk_fma_f32 v[72:73], v[74:75], s[20:21], v[72:73] op_sel_hi:[1,0,1]
	v_pk_add_f32 v[68:69], v[68:69], v[70:71]
	v_add_f32_e32 v74, v72, v78
	v_pk_mul_f32 v[68:69], v[68:69], s[22:23] op_sel_hi:[1,0]
	v_lshlrev_b32_e32 v70, 16, v10
	v_and_b32_e32 v71, 0xffff0000, v10
	v_cvt_pk_f32_fp8_sdwa v[56:57], v28 src0_sel:WORD_1
	v_cvt_pk_f32_fp8_sdwa v[58:59], v44 src0_sel:WORD_1
	v_add_f32_e32 v74, v73, v74
	v_pk_fma_f32 v[68:69], v[70:71], s[20:21], v[68:69] op_sel_hi:[1,0,1]
	v_pk_add_f32 v[64:65], v[64:65], v[66:67]
	v_add_f32_e32 v70, v68, v74
	v_pk_mul_f32 v[64:65], v[64:65], s[22:23] op_sel_hi:[1,0]
	v_lshlrev_b32_e32 v66, 16, v11
	v_and_b32_e32 v67, 0xffff0000, v11
	v_cvt_pk_f32_fp8_e32 v[52:53], v29
	v_cvt_pk_f32_fp8_e32 v[54:55], v45
	v_add_f32_e32 v70, v69, v70
	v_pk_fma_f32 v[64:65], v[66:67], s[20:21], v[64:65] op_sel_hi:[1,0,1]
	v_pk_add_f32 v[60:61], v[60:61], v[62:63]
	v_add_f32_e32 v66, v64, v70
	v_pk_mul_f32 v[60:61], v[60:61], s[22:23] op_sel_hi:[1,0]
	v_lshlrev_b32_e32 v62, 16, v12
	v_and_b32_e32 v63, 0xffff0000, v12
	v_cvt_pk_f32_fp8_sdwa v[48:49], v29 src0_sel:WORD_1
	v_cvt_pk_f32_fp8_sdwa v[50:51], v45 src0_sel:WORD_1
	v_add_f32_e32 v66, v65, v66
	v_pk_fma_f32 v[60:61], v[62:63], s[20:21], v[60:61] op_sel_hi:[1,0,1]
	v_pk_add_f32 v[56:57], v[56:57], v[58:59]
	v_add_f32_e32 v62, v60, v66
	v_pk_mul_f32 v[56:57], v[56:57], s[22:23] op_sel_hi:[1,0]
	v_lshlrev_b32_e32 v58, 16, v13
	v_and_b32_e32 v59, 0xffff0000, v13
	v_add_f32_e32 v62, v61, v62
	v_pk_fma_f32 v[56:57], v[58:59], s[20:21], v[56:57] op_sel_hi:[1,0,1]
	v_pk_add_f32 v[52:53], v[52:53], v[54:55]
	v_add_f32_e32 v58, v56, v62
	v_pk_mul_f32 v[52:53], v[52:53], s[22:23] op_sel_hi:[1,0]
	v_lshlrev_b32_e32 v54, 16, v14
	v_and_b32_e32 v55, 0xffff0000, v14
	v_and_b32_e32 v112, 64, v195
	v_add_f32_e32 v58, v57, v58
	v_pk_fma_f32 v[52:53], v[54:55], s[20:21], v[52:53] op_sel_hi:[1,0,1]
	v_pk_add_f32 v[48:49], v[48:49], v[50:51]
	v_add_u32_e32 v112, 64, v112
	v_xor_b32_e32 v113, 1, v195
	v_add_f32_e32 v54, v52, v58
	v_pk_mul_f32 v[48:49], v[48:49], s[22:23] op_sel_hi:[1,0]
	v_lshlrev_b32_e32 v50, 16, v15
	v_and_b32_e32 v51, 0xffff0000, v15
	v_cmp_lt_i32_e32 vcc, v113, v112
	v_add_f32_e32 v54, v53, v54
	v_pk_fma_f32 v[48:49], v[50:51], s[20:21], v[48:49] op_sel_hi:[1,0,1]
	v_cndmask_b32_e32 v113, v195, v113, vcc
	v_add_f32_e32 v50, v48, v54
	v_lshlrev_b32_e32 v113, 2, v113
	v_add_f32_e32 v50, v49, v50
	s_nop 1
	v_mov_b32_dpp v51, v50 quad_perm:[1,0,3,2] row_mask:0xf bank_mask:0xf
	v_xor_b32_e32 v54, 2, v195
	v_cmp_lt_i32_e32 vcc, v54, v112
	s_waitcnt lgkmcnt(0)
	v_add_f32_e32 v50, v50, v51
	v_cndmask_b32_e32 v54, v195, v54, vcc
	v_lshlrev_b32_e32 v86, 2, v54
	s_nop 1
	v_mov_b32_dpp v51, v50 quad_perm:[2,3,0,1] row_mask:0xf bank_mask:0xf
	v_xor_b32_e32 v54, 4, v195
	v_cmp_lt_i32_e32 vcc, v54, v112
	s_waitcnt lgkmcnt(0)
	v_add_f32_e32 v50, v50, v51
	v_cndmask_b32_e32 v54, v195, v54, vcc
	v_lshlrev_b32_e32 v87, 2, v54
	s_nop 1
	v_mov_b32_dpp v51, v50 row_half_mirror row_mask:0xf bank_mask:0xf
	v_xor_b32_e32 v54, 8, v195
	v_cmp_lt_i32_e32 vcc, v54, v112
	s_waitcnt lgkmcnt(0)
	v_add_f32_e32 v50, v50, v51
	v_cndmask_b32_e32 v54, v195, v54, vcc
	v_lshlrev_b32_e32 v90, 2, v54
	s_nop 1
	v_mov_b32_dpp v51, v50 row_mirror row_mask:0xf bank_mask:0xf
	v_xor_b32_e32 v54, 16, v195
	v_cmp_lt_i32_e32 vcc, v54, v112
	s_waitcnt lgkmcnt(0)
	v_add_f32_e32 v50, v50, v51
	v_cndmask_b32_e32 v54, v195, v54, vcc
	v_lshlrev_b32_e32 v91, 2, v54
	ds_bpermute_b32 v51, v91, v50
	v_xor_b32_e32 v54, 32, v195
	v_cmp_lt_i32_e32 vcc, v54, v112
	s_waitcnt lgkmcnt(0)
	v_add_f32_e32 v50, v50, v51
	v_cndmask_b32_e32 v54, v195, v54, vcc
	v_lshlrev_b32_e32 v94, 2, v54
	ds_bpermute_b32 v51, v94, v50
	s_waitcnt lgkmcnt(0)
	v_add_f32_e32 v50, v50, v51
	v_mul_f32_e32 v50, 0x3a000000, v50
	v_pk_add_f32 v[70:71], v[108:109], v[50:51] op_sel_hi:[1,0] neg_lo:[0,1] neg_hi:[0,1]
	v_pk_add_f32 v[78:79], v[104:105], v[50:51] op_sel_hi:[1,0] neg_lo:[0,1] neg_hi:[0,1]
	v_pk_mul_f32 v[54:55], v[70:71], v[70:71]
	v_pk_mul_f32 v[58:59], v[78:79], v[78:79]
	v_pk_add_f32 v[120:121], v[100:101], v[50:51] op_sel_hi:[1,0] neg_lo:[0,1] neg_hi:[0,1]
	v_pk_add_f32 v[122:123], v[96:97], v[50:51] op_sel_hi:[1,0] neg_lo:[0,1] neg_hi:[0,1]
	v_pk_add_f32 v[124:125], v[92:93], v[50:51] op_sel_hi:[1,0] neg_lo:[0,1] neg_hi:[0,1]
	v_pk_add_f32 v[126:127], v[88:89], v[50:51] op_sel_hi:[1,0] neg_lo:[0,1] neg_hi:[0,1]
	v_pk_add_f32 v[138:139], v[84:85], v[50:51] op_sel_hi:[1,0] neg_lo:[0,1] neg_hi:[0,1]
	v_pk_add_f32 v[156:157], v[80:81], v[50:51] op_sel_hi:[1,0] neg_lo:[0,1] neg_hi:[0,1]
	v_pk_add_f32 v[158:159], v[76:77], v[50:51] op_sel_hi:[1,0] neg_lo:[0,1] neg_hi:[0,1]
	v_pk_add_f32 v[160:161], v[72:73], v[50:51] op_sel_hi:[1,0] neg_lo:[0,1] neg_hi:[0,1]
	v_pk_add_f32 v[162:163], v[68:69], v[50:51] op_sel_hi:[1,0] neg_lo:[0,1] neg_hi:[0,1]
	v_pk_add_f32 v[164:165], v[64:65], v[50:51] op_sel_hi:[1,0] neg_lo:[0,1] neg_hi:[0,1]
	v_pk_add_f32 v[166:167], v[60:61], v[50:51] op_sel_hi:[1,0] neg_lo:[0,1] neg_hi:[0,1]
	v_pk_add_f32 v[168:169], v[56:57], v[50:51] op_sel_hi:[1,0] neg_lo:[0,1] neg_hi:[0,1]
	v_pk_add_f32 v[170:171], v[52:53], v[50:51] op_sel_hi:[1,0] neg_lo:[0,1] neg_hi:[0,1]
	v_pk_add_f32 v[172:173], v[48:49], v[50:51] op_sel_hi:[1,0] neg_lo:[0,1] neg_hi:[0,1]
	v_add_f32_e32 v50, v54, v55
	v_add_f32_e32 v50, v58, v50
	v_pk_mul_f32 v[62:63], v[120:121], v[120:121]
	v_add_f32_e32 v50, v59, v50
	v_add_f32_e32 v50, v62, v50
	v_pk_mul_f32 v[66:67], v[122:123], v[122:123]
	v_add_f32_e32 v50, v63, v50
	v_add_f32_e32 v50, v66, v50
	v_pk_mul_f32 v[74:75], v[124:125], v[124:125]
	v_add_f32_e32 v50, v67, v50
	v_add_f32_e32 v50, v74, v50
	v_pk_mul_f32 v[82:83], v[126:127], v[126:127]
	v_add_f32_e32 v50, v75, v50
	v_add_f32_e32 v50, v82, v50
	v_pk_mul_f32 v[84:85], v[138:139], v[138:139]
	v_add_f32_e32 v50, v83, v50
	v_add_f32_e32 v50, v84, v50
	v_pk_mul_f32 v[80:81], v[156:157], v[156:157]
	v_add_f32_e32 v50, v85, v50
	v_add_f32_e32 v50, v80, v50
	v_pk_mul_f32 v[76:77], v[158:159], v[158:159]
	v_add_f32_e32 v50, v81, v50
	v_add_f32_e32 v50, v76, v50
	v_pk_mul_f32 v[72:73], v[160:161], v[160:161]
	v_add_f32_e32 v50, v77, v50
	v_add_f32_e32 v50, v72, v50
	v_pk_mul_f32 v[68:69], v[162:163], v[162:163]
	v_add_f32_e32 v50, v73, v50
	v_add_f32_e32 v50, v68, v50
	v_pk_mul_f32 v[64:65], v[164:165], v[164:165]
	v_add_f32_e32 v50, v69, v50
	v_add_f32_e32 v50, v64, v50
	v_pk_mul_f32 v[60:61], v[166:167], v[166:167]
	v_add_f32_e32 v50, v65, v50
	v_add_f32_e32 v50, v60, v50
	v_pk_mul_f32 v[56:57], v[168:169], v[168:169]
	v_add_f32_e32 v50, v61, v50
	v_add_f32_e32 v50, v56, v50
	v_pk_mul_f32 v[52:53], v[170:171], v[170:171]
	v_add_f32_e32 v50, v57, v50
	v_add_f32_e32 v50, v52, v50
	v_pk_mul_f32 v[48:49], v[172:173], v[172:173]
	v_add_f32_e32 v50, v53, v50
	v_add_f32_e32 v48, v48, v50
	v_add_f32_e32 v48, v49, v48
	s_nop 1
	v_mov_b32_dpp v49, v48 quad_perm:[1,0,3,2] row_mask:0xf bank_mask:0xf
	s_waitcnt lgkmcnt(0)
	v_add_f32_e32 v48, v48, v49
	s_nop 1
	v_mov_b32_dpp v49, v48 quad_perm:[2,3,0,1] row_mask:0xf bank_mask:0xf
	s_waitcnt lgkmcnt(0)
	v_add_f32_e32 v48, v48, v49
	s_nop 1
	v_mov_b32_dpp v49, v48 row_half_mirror row_mask:0xf bank_mask:0xf
	s_waitcnt lgkmcnt(0)
	v_add_f32_e32 v48, v48, v49
	s_nop 1
	v_mov_b32_dpp v49, v48 row_mirror row_mask:0xf bank_mask:0xf
	s_waitcnt lgkmcnt(0)
	v_add_f32_e32 v64, v48, v49
	ds_bpermute_b32 v65, v91, v64
	ds_read_b128 v[48:51], v134
	ds_read_b128 v[52:55], v135
	ds_read_b128 v[56:59], v136
	ds_read_b128 v[60:63], v142
	s_waitcnt lgkmcnt(4)
	v_add_f32_e32 v68, v64, v65
	ds_bpermute_b32 v69, v94, v68
	ds_read_b128 v[64:67], v143
	ds_read_b128 v[80:83], v144
	ds_read_b128 v[72:75], v145
	ds_read_b128 v[84:87], v146
	ds_read_b128 v[88:91], v147
	ds_read_b128 v[92:95], v148
	ds_read_b128 v[96:99], v149
	ds_read_b128 v[100:103], v150
	ds_read_b128 v[104:107], v151
	ds_read_b128 v[108:111], v152
	ds_read_b128 v[112:115], v153
	ds_read_b128 v[116:119], v154
	s_waitcnt lgkmcnt(12)
	v_add_f32_e32 v68, v68, v69
	v_fmamk_f32 v68, v68, 0x3a000000, v192
	v_mul_f32_e32 v69, 0x4f800000, v68
	v_cmp_gt_f32_e32 vcc, s88, v68
	s_nop 1
	v_cndmask_b32_e32 v68, v68, v69, vcc
	v_sqrt_f32_e32 v69, v68
	s_nop 0
	v_add_u32_e32 v76, -1, v69
	v_fma_f32 v77, -v76, v69, v68
	v_cmp_ge_f32_e64 s[36:37], 0, v77
	v_add_u32_e32 v77, 1, v69
	s_nop 0
	v_cndmask_b32_e64 v76, v69, v76, s[36:37]
	v_fma_f32 v69, -v77, v69, v68
	v_cmp_lt_f32_e64 s[36:37], 0, v69
	s_nop 1
	v_cndmask_b32_e64 v69, v76, v77, s[36:37]
	v_mul_f32_e32 v76, 0x37800000, v69
	v_cndmask_b32_e32 v69, v69, v76, vcc
	v_cmp_class_f32_e32 vcc, v68, v191
	s_nop 1
	v_cndmask_b32_e32 v68, v69, v68, vcc
	v_div_scale_f32 v69, s[10:11], v68, v68, 1.0
	v_rcp_f32_e32 v76, v69
	s_mov_b64 s[10:11], -1
	v_fma_f32 v77, -v69, v76, 1.0
	v_fmac_f32_e32 v76, v77, v76
	v_div_scale_f32 v77, vcc, 1.0, v68, 1.0
	v_mul_f32_e32 v155, v77, v76
	v_fma_f32 v174, -v69, v155, v77
	v_fmac_f32_e32 v155, v174, v76
	v_fma_f32 v69, -v69, v155, v77
	v_div_fmas_f32 v69, v69, v76, v155
	v_div_fixup_f32 v174, v69, v68, 1.0
	v_pk_mul_f32 v[68:69], v[70:71], v[174:175] op_sel_hi:[1,0]
	v_pk_mul_f32 v[70:71], v[120:121], v[174:175] op_sel_hi:[1,0]
	v_pk_fma_f32 v[76:77], v[48:49], v[68:69], v[56:57]
	v_pk_mul_f32 v[48:49], v[78:79], v[174:175] op_sel_hi:[1,0]
	v_pk_fma_f32 v[68:69], v[52:53], v[70:71], v[60:61]
	v_pk_fma_f32 v[78:79], v[50:51], v[48:49], v[58:59]
	v_pk_mul_f32 v[48:49], v[124:125], v[174:175] op_sel_hi:[1,0]
	v_pk_mul_f32 v[50:51], v[138:139], v[174:175] op_sel_hi:[1,0]
	s_waitcnt lgkmcnt(9)
	v_pk_fma_f32 v[72:73], v[64:65], v[48:49], v[72:73]
	s_waitcnt lgkmcnt(8)
	v_pk_fma_f32 v[64:65], v[80:81], v[50:51], v[84:85]
	v_pk_mul_f32 v[48:49], v[126:127], v[174:175] op_sel_hi:[1,0]
	v_pk_mul_f32 v[50:51], v[156:157], v[174:175] op_sel_hi:[1,0]
	v_pk_mul_f32 v[52:53], v[122:123], v[174:175] op_sel_hi:[1,0]
	v_pk_fma_f32 v[74:75], v[66:67], v[48:49], v[74:75]
	v_pk_fma_f32 v[66:67], v[82:83], v[50:51], v[86:87]
	v_pk_mul_f32 v[48:49], v[158:159], v[174:175] op_sel_hi:[1,0]
	v_pk_mul_f32 v[50:51], v[162:163], v[174:175] op_sel_hi:[1,0]
	v_pk_fma_f32 v[70:71], v[54:55], v[52:53], v[62:63]
	s_waitcnt lgkmcnt(5)
	v_pk_fma_f32 v[60:61], v[88:89], v[48:49], v[96:97]
	s_waitcnt lgkmcnt(4)
	v_pk_fma_f32 v[52:53], v[92:93], v[50:51], v[100:101]
	v_pk_mul_f32 v[48:49], v[160:161], v[174:175] op_sel_hi:[1,0]
	v_pk_mul_f32 v[50:51], v[164:165], v[174:175] op_sel_hi:[1,0]
	v_pk_fma_f32 v[62:63], v[90:91], v[48:49], v[98:99]
	v_pk_fma_f32 v[54:55], v[94:95], v[50:51], v[102:103]
	v_pk_mul_f32 v[48:49], v[166:167], v[174:175] op_sel_hi:[1,0]
	v_pk_mul_f32 v[50:51], v[170:171], v[174:175] op_sel_hi:[1,0]
	s_waitcnt lgkmcnt(1)
	v_pk_fma_f32 v[56:57], v[104:105], v[48:49], v[112:113]
	s_waitcnt lgkmcnt(0)
	v_pk_fma_f32 v[48:49], v[108:109], v[50:51], v[116:117]
	v_pk_mul_f32 v[50:51], v[168:169], v[174:175] op_sel_hi:[1,0]
	v_pk_mul_f32 v[80:81], v[172:173], v[174:175] op_sel_hi:[1,0]
	v_pk_fma_f32 v[58:59], v[106:107], v[50:51], v[114:115]
	v_pk_fma_f32 v[50:51], v[110:111], v[80:81], v[118:119]
	s_andn2_b64 vcc, exec, s[8:9]
	s_cbranch_vccnz .LBB0_1583
	s_ashr_i32 s7, s6, 31
	s_lshl_b64 s[10:11], s[6:7], 12
	v_lshl_add_u64 v[84:85], v[130:131], 0, s[10:11]
	v_cvt_pk_bf16_f32 v80, v76, v77
	v_cvt_pk_bf16_f32 v81, v78, v79
	v_cvt_pk_bf16_f32 v82, v68, v69
	v_cvt_pk_bf16_f32 v83, v70, v71
	global_store_dwordx4 v[84:85], v[80:83], off
	s_mov_b64 s[10:11], 0
	s_nop 0
	v_cvt_pk_bf16_f32 v80, v72, v73
	v_cvt_pk_bf16_f32 v81, v74, v75
	v_cvt_pk_bf16_f32 v82, v64, v65
	v_cvt_pk_bf16_f32 v83, v66, v67
	global_store_dwordx4 v[84:85], v[80:83], off offset:1024
	s_nop 1
	v_cvt_pk_bf16_f32 v80, v60, v61
	v_cvt_pk_bf16_f32 v81, v62, v63
	v_cvt_pk_bf16_f32 v82, v52, v53
	v_cvt_pk_bf16_f32 v83, v54, v55
	global_store_dwordx4 v[84:85], v[80:83], off offset:2048
	s_nop 1
	v_cvt_pk_bf16_f32 v80, v56, v57
	v_cvt_pk_bf16_f32 v81, v58, v59
	v_cvt_pk_bf16_f32 v82, v48, v49
	v_cvt_pk_bf16_f32 v83, v50, v51
	global_store_dwordx4 v[84:85], v[80:83], off offset:3072
